# MoE1 unit start: the 4 serialized gather-index loads issued together under one wait (on top of MoE epilogue batching)
# speedup vs baseline: 1.0077x; 1.0077x over previous
;     __device__ __forceinline__ void a_voff(const Unit& u, const int (&R)[2], const int (&C)[2], unsigned (&v)[2][2]) const {
;         if (PHASE == 1) {
;             const int cnt = tab[80 + u.a0];
; #pragma unroll
;             for (int h = 0; h < 2; ++h)
; #pragma unroll
;                 for (int i = 0; i < 2; ++i) { const int rank = u.a1 * BM + h * HALF + R[i]; const int tok = rank < cnt ? ltok[(size_t)u.a0 * NTOK + rank] : 0; v[h][i] = (unsigned)(tok * DM + C[i]) * 2u; }
.LBB0_905:
	v_cndmask_b32_e64 v2, 0, 1, s[22:23]
	v_cmp_ne_u32_e64 s[4:5], 1, v2
	s_andn2_b64 vcc, exec, s[22:23]
	s_mov_b64 s[22:23], s[28:29]
	v_mov_b32_e32 v161, v140
	v_mov_b32_e32 v158, v134
	v_mov_b32_e32 v159, v136
	v_mov_b32_e32 v160, v138
	s_cbranch_vccnz .LBB0_915
	s_lshl_b32 s19, s18, 2
	s_add_i32 s19, s19, 0
	s_add_i32 s19, s19, 0x24140
	v_mov_b32_e32 v2, s19
	ds_read_b32 v8, v2
	v_lshlrev_b32_e32 v9, 8, v157
	v_or_b32_e32 v11, 0x80, v9
	v_add_u32_e32 v20, v9, v147
	v_add_u32_e32 v21, v9, v149
	v_add_u32_e32 v22, v11, v147
	v_add_u32_e32 v23, v11, v149
	s_ashr_i32 s19, s18, 31
	s_lshl_b64 s[30:31], s[18:19], 18
	s_add_u32 s30, s41, s30
	s_addc_u32 s31, s42, s31
	v_mov_b32_e32 v13, 0
	v_mov_b32_e32 v15, 0
	v_mov_b32_e32 v17, 0
	v_mov_b32_e32 v19, 0
	s_waitcnt lgkmcnt(0)
	v_cmp_lt_i32_e32 vcc, v20, v8
	s_nop 1
	v_cndmask_b32_e32 v12, 0, v20, vcc
	v_cmp_lt_i32_e32 vcc, v21, v8
	s_nop 1
	v_cndmask_b32_e32 v14, 0, v21, vcc
	v_cmp_lt_i32_e32 vcc, v22, v8
	s_nop 1
	v_cndmask_b32_e32 v16, 0, v22, vcc
	v_cmp_lt_i32_e32 vcc, v23, v8
	s_nop 1
	v_cndmask_b32_e32 v18, 0, v23, vcc
	v_lshl_add_u64 v[12:13], v[12:13], 2, s[30:31]
	v_lshl_add_u64 v[14:15], v[14:15], 2, s[30:31]
	v_lshl_add_u64 v[16:17], v[16:17], 2, s[30:31]
	v_lshl_add_u64 v[18:19], v[18:19], 2, s[30:31]
	global_load_dword v7, v[12:13], off
	global_load_dword v6, v[14:15], off
	global_load_dword v10, v[16:17], off
	global_load_dword v9, v[18:19], off
	s_waitcnt vmcnt(0)
	v_cmp_lt_i32_e32 vcc, v20, v8
	v_lshlrev_b32_e32 v7, 10, v7
	v_lshlrev_b32_e32 v6, 10, v6
	v_cndmask_b32_e32 v7, 0, v7, vcc
	v_cmp_lt_i32_e32 vcc, v21, v8
	v_lshlrev_b32_e32 v10, 10, v10
	v_lshlrev_b32_e32 v9, 10, v9
	v_cndmask_b32_e32 v6, 0, v6, vcc
	v_cmp_lt_i32_e32 vcc, v22, v8
	s_nop 1
	v_cndmask_b32_e32 v10, 0, v10, vcc
	v_cmp_lt_i32_e32 vcc, v23, v8
	s_nop 1
	v_cndmask_b32_e32 v9, 0, v9, vcc
	s_lshl_b32 s19, s18, 21
	s_ashr_i32 s21, s20, 31
	s_and_b32 s19, s19, 0x3e00000
	s_lshl_b64 s[22:23], s[20:21], 19
	s_add_u32 s21, s43, s22
	s_addc_u32 s23, s44, s23
	s_add_u32 s22, s21, s19
	v_add_lshl_u32 v158, v10, v153, 1
	v_add_lshl_u32 v159, v6, v154, 1
	v_add_lshl_u32 v160, v7, v153, 1
	s_addc_u32 s23, s23, 0
	v_add_lshl_u32 v161, v9, v154, 1
